# baseline (speedup 1.0000x reference)
.Lstag_done_p3:
	s_mov_b32 s66, s2
	s_load_dwordx2 s[64:65], s[0:1], 0x0
	v_lshrrev_b32_e32 v162, 6, v0
	v_bfe_u32 v163, v0, 2, 4
	v_lshl_add_u32 v162, v162, 7, v163
	v_lshlrev_b32_e32 v163, 4, v0
	v_and_b32_e32 v163, 48, v163
	v_lshl_add_u32 v162, v162, 9, v163
	s_load_dwordx8 s[4:11], s[0:1], 0x0
	s_load_dwordx2 s[16:17], s[0:1], 0x20
	s_load_dwordx4 s[12:15], s[0:1], 0x30
	s_ashr_i32 s0, s2, 3
	s_mul_hi_i32 s18, s0, 0x55555556
	s_lshr_b32 s19, s18, 31
	s_add_i32 s21, s18, s19
	s_mul_i32 s18, s21, 0x3fffffd
	s_bfe_u32 s1, s2, 0x20001
	s_add_i32 s18, s18, s0
	s_lshl_b32 s2, s2, 5
	s_lshl_b32 s0, s18, 6
	s_and_b32 s2, s2, 32
	s_or_b32 s0, s0, s2
	s_lshl_b32 s2, s21, 1
	s_and_b32 s19, s2, -16
	s_lshl_b32 s2, s21, 4
	s_and_b32 s20, s2, 0x70
	s_mul_i32 s2, s1, 0xc0
	s_add_i32 s18, s0, s2
	s_mov_b32 s3, 0
	v_mov_b32_e32 v50, 0
	v_lshrrev_b32_e32 v142, 6, v0
	v_bfe_u32 v45, v0, 2, 4
	v_lshlrev_b32_e32 v1, 4, v0
	v_and_b32_e32 v34, 48, v1
	v_lshl_add_u32 v1, v142, 7, v45
	v_lshl_add_u32 v1, v1, 9, v34
	s_lshl_b32 s22, s18, 7
	s_add_i32 s22, s22, s19
	s_lshl_b32 s22, s22, 9
	s_lshl_b32 s2, s20, 2
	s_add_i32 s22, s22, s2
	s_waitcnt lgkmcnt(0)
	s_add_u32 s24, s4, s22
	s_addc_u32 s25, s5, 0
	s_add_u32 s26, s24, 0x40000
	s_addc_u32 s27, s25, 0
	s_add_u32 s28, s26, 0x40000
	s_addc_u32 s29, s27, 0
	s_add_u32 s30, s28, 0x40000
	s_addc_u32 s31, s29, 0
	s_add_u32 s32, s30, 0x40000
	s_addc_u32 s33, s31, 0
	s_add_u32 s34, s32, 0x40000
	s_addc_u32 s35, s33, 0
	s_add_u32 s36, s34, 0x40000
	s_addc_u32 s37, s35, 0
	s_add_u32 s38, s36, 0x40000
	s_addc_u32 s39, s37, 0
	v_readfirstlane_b32 s23, v142
	s_nop 3
	s_mul_i32 s23, s23, 0x410
	s_add_i32 m0, s23, 29120
	s_nop 0
	global_load_lds_dwordx4 v1, s[38:39]
	s_add_i32 m0, s23, 24960
	s_nop 0
	global_load_lds_dwordx4 v1, s[36:37]
	s_add_i32 m0, s23, 20800
	s_nop 0
	global_load_lds_dwordx4 v1, s[34:35]
	s_add_i32 m0, s23, 16640
	s_nop 0
	global_load_lds_dwordx4 v1, s[32:33]
	s_add_i32 m0, s23, 12480
	s_nop 0
	global_load_lds_dwordx4 v1, s[30:31]
	s_add_i32 m0, s23, 8320
	s_nop 0
	global_load_lds_dwordx4 v1, s[28:29]
	v_and_b32_e32 v35, 31, v0
	s_add_i32 m0, s23, 4160
	s_nop 0
	global_load_lds_dwordx4 v1, s[26:27]
	s_mov_b32 m0, s23
	s_nop 0
	global_load_lds_dwordx4 v1, s[24:25]
	v_or_b32_e32 v36, s0, v35
	v_ashrrev_i32_e32 v37, 31, v36
	v_lshlrev_b64 v[38:39], 2, v[36:37]
	v_lshlrev_b32_e32 v89, 1, v142
	v_and_b32_e32 v1, 3, v0
	v_lshrrev_b32_e32 v37, 1, v0
	v_lshl_add_u64 v[40:41], s[16:17], 0, v[38:39]
	v_and_or_b32 v144, v37, 12, v1
	v_or_b32_e32 v1, s20, v89
	global_load_dword v94, v[40:41], off
	v_bfe_u32 v143, v0, 2, 1
	v_lshlrev_b32_e32 v40, 1, v35
	v_mov_b32_e32 v41, v50
	v_or_b32_e32 v37, 8, v1
	v_bfe_u32 v95, v0, 5, 1
	s_lshl_b32 s4, s1, 16
	s_mov_b64 s[68:69], s[6:7]
	s_mov_b64 s[70:71], s[12:13]
	v_lshlrev_b32_e32 v155, 1, v35
	v_lshl_add_u64 v[86:87], s[12:13], 0, v[40:41]
	v_or_b32_e32 v51, s19, v144
	v_or_b32_e32 v40, v37, v143
	v_lshlrev_b32_e32 v82, 4, v95
	v_mov_b32_e32 v83, v50
	s_ashr_i32 s5, s0, 5
	s_or_b32 s0, s4, 0x4000
	v_lshl_add_u32 v42, v40, 7, v51
	v_lshl_add_u64 v[84:85], s[6:7], 0, v[82:83]
	s_or_b32 s2, s4, 0xc000
	s_mul_i32 s7, s1, 24
	v_add_u32_e32 v40, s0, v42
	s_or_b32 s1, s7, 6
	v_ashrrev_i32_e32 v41, 31, v40
	v_add_u32_e32 v42, s2, v42
	s_add_i32 s6, s5, 12
	s_ashr_i32 s12, s21, 3
	s_add_i32 s13, s1, s5
	v_lshlrev_b64 v[40:41], 5, v[40:41]
	v_ashrrev_i32_e32 v43, 31, v42
	v_or_b32_e32 v37, v37, v95
	s_lshl_b32 s13, s13, 10
	s_add_i32 s1, s1, s6
	v_lshl_add_u64 v[40:41], v[84:85], 0, v[40:41]
	v_lshlrev_b64 v[42:43], 5, v[42:43]
	v_lshl_add_u32 v37, v37, 3, s12
	s_lshl_b32 s1, s1, 10
	v_lshl_add_u64 v[42:43], v[84:85], 0, v[42:43]
	global_load_dwordx4 v[58:61], v[40:41], off
	global_load_dwordx4 v[62:65], v[42:43], off
	v_add_u32_e32 v40, s13, v37
	v_ashrrev_i32_e32 v41, 31, v40
	v_add_u32_e32 v42, s1, v37
	v_lshlrev_b64 v[40:41], 6, v[40:41]
	v_ashrrev_i32_e32 v43, 31, v42
	v_lshl_or_b32 v88, v36, 1, v95
	v_lshl_add_u64 v[40:41], v[86:87], 0, v[40:41]
	v_lshlrev_b64 v[42:43], 6, v[42:43]
	v_add_u32_e32 v36, 0x180, v88
	v_lshl_add_u64 v[42:43], v[86:87], 0, v[42:43]
	global_load_ushort v145, v[40:41], off
	global_load_ushort v146, v[42:43], off
	v_ashrrev_i32_e32 v37, 31, v36
	v_add_u32_e32 v40, 0x480, v88
	v_lshl_add_u64 v[36:37], v[36:37], 4, s[8:9]
	v_ashrrev_i32_e32 v41, 31, v40
	v_lshl_add_u64 v[40:41], v[40:41], 4, s[8:9]
	global_load_dwordx4 v[66:69], v[36:37], off
	global_load_dwordx4 v[70:73], v[40:41], off
	v_or_b32_e32 v36, v1, v95
	v_lshl_add_u64 v[90:91], s[10:11], 0, v[38:39]
	v_lshl_add_u32 v38, v36, 3, s12
	v_add_u32_e32 v36, s1, v38
	v_ashrrev_i32_e32 v37, 31, v36
	v_add_u32_e32 v38, s13, v38
	v_lshlrev_b64 v[36:37], 6, v[36:37]
	v_ashrrev_i32_e32 v39, 31, v38
	v_or_b32_e32 v1, v1, v143
	v_lshl_add_u64 v[36:37], v[86:87], 0, v[36:37]
	v_lshlrev_b64 v[38:39], 6, v[38:39]
	v_lshl_add_u32 v1, v1, 7, v51
	global_load_dword v92, v[90:91], off offset:2304
	global_load_dword v96, v[90:91], off offset:768
	v_lshl_add_u64 v[38:39], v[86:87], 0, v[38:39]
	global_load_ushort v150, v[36:37], off
	global_load_ushort v151, v[38:39], off
	v_add_u32_e32 v36, s2, v1
	v_ashrrev_i32_e32 v37, 31, v36
	v_add_u32_e32 v38, s0, v1
	v_lshlrev_b64 v[36:37], 5, v[36:37]
	v_ashrrev_i32_e32 v39, 31, v38
	v_lshl_add_u64 v[36:37], v[84:85], 0, v[36:37]
	v_lshlrev_b64 v[38:39], 5, v[38:39]
	v_lshl_add_u64 v[38:39], v[84:85], 0, v[38:39]
	global_load_dwordx4 v[74:77], v[36:37], off
	global_load_dwordx4 v[78:81], v[38:39], off
	v_and_b32_e32 v1, 63, v0
	v_cmp_gt_u32_e32 vcc, 32, v1
	v_bfrev_b32_e32 v1, 60
	v_mul_u32_u24_e32 v83, 0x210, v35
	v_mov_b32_e32 v36, 0x3c00
	v_cndmask_b32_e64 v56, v1, 0, vcc
	v_mul_u32_u24_e32 v1, 0x410, v35
	v_lshl_or_b32 v35, v95, 1, v83
	v_cndmask_b32_e64 v53, v36, 0, vcc
	v_add_u32_e32 v148, 0x8200, v35
	v_mul_u32_u24_e32 v35, 0x410, v142
	v_lshlrev_b32_e32 v36, 6, v45
	v_add3_u32 v34, v35, v36, v34
	s_waitcnt vmcnt(13)
	s_waitcnt lgkmcnt(0)
	s_barrier
	v_mov_b32_e32 v51, v50
	v_mov_b32_e32 v52, v50
	v_mov_b32_e32 v54, v50
	v_mov_b32_e32 v55, v50
	v_mov_b32_e32 v57, v50
	v_lshl_or_b32 v147, v95, 2, v1
	s_mov_b64 s[0:1], -1
	s_mov_b32 s10, 0x7f61b1e6
	s_mov_b32 s11, 0x42800000
	s_waitcnt vmcnt(5)
	v_mov_b32_e32 v93, v92
	s_waitcnt vmcnt(4)
	v_mov_b32_e32 v97, v96
	s_branch .LBB3_3

.LBB3_10:
	v_add_u32_e32 v6, s19, v89
	v_add_u32_e32 v8, 8, v6
	v_or_b32_e32 v7, s20, v144
	v_or_b32_e32 v2, v8, v143
	v_lshl_or_b32 v4, v2, 7, v7
	s_or_b32 s0, s4, 0x8000
	v_add_u32_e32 v2, s4, v4
	v_add_u32_e32 v4, s0, v4
	v_lshl_add_u32 v2, v2, 5, v82
	v_lshl_add_u32 v4, v4, 5, v82
	s_lshr_b32 s1, s20, 4
	s_add_i32 s2, s7, s5
	s_add_i32 s7, s7, s6
	global_load_dwordx4 v[58:61], v2, s[68:69]
	global_load_dwordx4 v[62:65], v4, s[68:69]
	v_or_b32_e32 v2, v8, v95
	s_lshl_b32 s2, s2, 10
	s_lshl_b32 s3, s7, 10
	v_lshl_or_b32 v4, v2, 3, s1
	v_add_u32_e32 v2, s2, v4
	v_add_u32_e32 v4, s3, v4
	v_lshl_add_u32 v2, v2, 6, v155
	v_lshl_add_u32 v4, v4, 6, v155
	global_load_ushort v132, v2, s[70:71]
	global_load_ushort v133, v4, s[70:71]
	v_add_u32_e32 v4, 0x300, v88
	v_lshlrev_b32_e32 v2, 4, v88
	v_lshlrev_b32_e32 v4, 4, v4
	global_load_dwordx4 v[66:69], v2, s[8:9]
	global_load_dwordx4 v[70:73], v4, s[8:9]
	global_load_dword v96, v[90:91], off
	global_load_dword v98, v[90:91], off offset:1536
	v_or_b32_e32 v2, v6, v95
	v_lshl_or_b32 v4, v2, 3, s1
	v_add_u32_e32 v2, s3, v4
	v_add_u32_e32 v4, s2, v4
	v_lshl_add_u32 v2, v2, 6, v155
	v_lshl_add_u32 v4, v4, 6, v155
	global_load_ushort v138, v2, s[70:71]
	global_load_ushort v139, v4, s[70:71]
	v_or_b32_e32 v2, v6, v143
	v_lshl_or_b32 v4, v2, 7, v7
	v_add_u32_e32 v2, s0, v4
	v_add_u32_e32 v4, s4, v4
	v_lshl_add_u32 v2, v2, 5, v82
	v_lshl_add_u32 v4, v4, 5, v82
	global_load_dwordx4 v[90:93], v2, s[68:69]
	global_load_dwordx4 v[18:21], v4, s[68:69]
	v_lshl_or_b32 v134, v142, 5, v82
	v_add_u32_e32 v135, 0x8200, v83
	v_mov_b32_e32 v95, v94
	s_mov_b32 s6, 0
	s_mov_b64 s[0:1], -1
	s_mov_b32 s4, 0x7f61b1e6
	s_mov_b32 s5, 0x42800000
	s_waitcnt vmcnt(5)
	v_mov_b32_e32 v97, v96
	s_waitcnt vmcnt(4)
	v_mov_b32_e32 v99, v98
	s_waitcnt vmcnt(0)
	s_branch .LBB3_12
